# attention main loops (window + selected): one static s_setprio 1 for waves 4-7 before the block loop, reset to 0 after it
# baseline (speedup 1.0000x reference)
.LBB0_591:
	s_cmp_ge_i32 s13, s30
	s_cselect_b64 s[0:1], -1, 0
	s_cmp_ge_i32 s82, s88
	s_cselect_b64 s[2:3], -1, 0
	s_or_b64 s[0:1], s[2:3], s[0:1]
	s_and_b64 vcc, exec, s[0:1]
	s_cbranch_vccnz .LBB0_765
	s_ashr_i32 s0, s13, 3
	s_mul_hi_i32 s1, s0, 0x92492493
	s_add_i32 s1, s1, s0
	s_lshr_b32 s2, s1, 31
	s_ashr_i32 s1, s1, 4
	s_add_i32 s1, s1, s2
	s_mul_i32 s2, s1, 0xffffffe4
	s_add_i32 s2, s2, s0
	s_mul_hi_i32 s0, s2, 0x92492493
	s_add_i32 s0, s0, s2
	s_lshr_b32 s3, s0, 31
	s_ashr_i32 s0, s0, 4
	s_add_i32 s0, s0, s3
	s_mul_i32 s3, s0, 28
	s_sub_i32 s2, s2, s3
	s_sub_i32 s31, 31, s2
	s_sub_i32 s3, s2, 24
	s_cmp_lt_i32 s2, 24
	s_cselect_b32 s10, s31, s3
	s_lshl_b32 s1, s1, 3
	s_and_b32 s2, s13, 7
	s_or_b32 s1, s1, s2
	s_add_i32 s33, s1, s0
	s_ashr_i32 s0, s33, 2
	s_ashr_i32 s1, s0, 31
	s_ashr_i32 s11, s10, 31
	s_and_b32 s6, s33, 3
	s_lshl_b64 s[2:3], s[0:1], 11
	s_lshl_b64 s[4:5], s[10:11], 6
	s_add_u32 s2, s2, s4
	s_addc_u32 s3, s3, s5
	s_mul_i32 s1, s3, 0x8a00
	s_mul_hi_u32 s4, s2, 0x8a00
	s_add_i32 s4, s4, s1
	s_mul_i32 s1, s2, 0x8a00
	s_add_u32 s1, s96, s1
	s_addc_u32 s4, s97, s4
	s_lshl_b32 s5, s6, 10
	s_add_u32 s1, s1, s5
	s_addc_u32 s4, s4, 0
	s_add_u32 s36, s1, 0x4000
	s_addc_u32 s37, s4, 0
	s_mul_hi_i32 s1, s0, 0x4500000
	s_mul_i32 s0, s0, 0x4500000
	s_add_u32 s0, s96, s0
	s_addc_u32 s1, s97, s1
	s_lshl_b32 s4, s6, 8
	s_add_u32 s0, s0, s4
	s_addc_u32 s1, s1, 0
	s_add_u32 s24, s0, 0x6000
	s_addc_u32 s25, s1, 0
	s_add_u32 s26, s0, 0x6400
	s_addc_u32 s27, s1, 0
	s_add_u32 s34, s86, 0x7000000
	s_addc_u32 s35, s87, 0
	s_lshl_b64 s[0:1], s[2:3], 12
	s_add_u32 s0, s34, s0
	s_addc_u32 s1, s35, s1
	s_add_u32 s22, s0, s5
	v_readfirstlane_b32 s2, v254
	s_addc_u32 s23, s1, 0
	s_and_b32 s0, s2, 0xffffff80
	v_and_b32_e32 v194, 31, v254
	s_ashr_i32 s1, s0, 31
	s_lshr_b32 s2, s2, 1
	s_lshl_b32 s49, s10, 6
	v_and_or_b32 v0, s2, 32, v194
	s_lshl_b64 s[0:1], s[0:1], 1
	v_mul_u32_u24_e32 v0, 0x4500, v0
	s_add_u32 s0, s36, s0
	s_addc_u32 s1, s37, s1
	v_lshlrev_b32_e32 v196, 1, v0
	v_mov_b32_e32 v197, 0
	v_lshl_add_u64 v[0:1], s[0:1], 0, v[196:197]
	s_add_i32 s0, s49, 0xfffffe01
	s_waitcnt vmcnt(0)
	v_lshrrev_b32_e32 v2, 1, v254
	s_andn2_b32 s0, s0, 63
	v_and_b32_e32 v196, 16, v2
	s_cmp_gt_i32 s10, 7
	v_lshl_add_u64 v[2:3], v[0:1], 0, v[196:197]
	s_cselect_b32 s0, s0, 0
	v_lshrrev_b32_e32 v1, 4, v254
	v_lshlrev_b32_e32 v0, 3, v254
	s_mov_b32 s11, 0x8a00
	v_and_b32_e32 v198, 0x78, v0
	v_or_b32_e32 v8, s0, v1
	v_or_b32_e32 v195, 32, v1
	v_mov_b64_e32 v[4:5], s[24:25]
	v_lshlrev_b32_e32 v196, 1, v198
	v_or_b32_e32 v9, s0, v195
	v_mad_u64_u32 v[6:7], s[0:1], v8, s11, v[4:5]
	v_lshl_add_u64 v[6:7], v[6:7], 0, v[196:197]
	v_mad_u64_u32 v[4:5], s[0:1], v9, s11, v[4:5]
	v_lshl_add_u64 v[4:5], v[4:5], 0, v[196:197]
	global_load_dwordx4 v[98:101], v[6:7], off
	global_load_dwordx4 v[102:105], v[4:5], off
	global_load_dwordx4 v[158:161], v[2:3], off
	global_load_dwordx4 v[154:157], v[2:3], off offset:32
	global_load_dwordx4 v[150:153], v[2:3], off offset:64
	global_load_dwordx4 v[146:149], v[2:3], off offset:96
	global_load_dwordx4 v[142:145], v[2:3], off offset:128
	global_load_dwordx4 v[138:141], v[2:3], off offset:160
	global_load_dwordx4 v[134:137], v[2:3], off offset:192
	global_load_dwordx4 v[130:133], v[2:3], off offset:224
	v_mov_b64_e32 v[4:5], s[26:27]
	v_mad_u64_u32 v[2:3], s[0:1], v8, s11, v[4:5]
	v_mad_u64_u32 v[4:5], s[0:1], v9, s11, v[4:5]
	v_lshl_add_u64 v[2:3], v[2:3], 0, v[196:197]
	v_lshl_add_u64 v[4:5], v[4:5], 0, v[196:197]
	global_load_dwordx4 v[106:109], v[2:3], off
	global_load_dwordx4 v[110:113], v[4:5], off
	s_movk_i32 s0, 0x70
	v_lshrrev_b32_e32 v5, 3, v254
	v_lshlrev_b32_e32 v7, 8, v1
	v_and_b32_e32 v5, 8, v5
	v_bitop3_b32 v9, v196, v254, s0 bitop3:0x78
	v_and_or_b32 v8, v1, 16, v5
	v_add3_u32 v9, 0, v7, v9
	v_and_or_b32 v5, v195, 48, v5
	v_lshrrev_b32_e32 v6, 5, v254
	v_lshrrev_b32_e32 v8, 1, v8
	s_waitcnt vmcnt(0)
	v_bfe_u32 v10, v254, 4, 2
	v_lshrrev_b32_e32 v5, 1, v5
	v_and_or_b32 v6, v6, 4, v10
	v_lshlrev_b32_e32 v6, 6, v6
	v_and_b32_e32 v10, 48, v196
	v_and_b32_e32 v2, 0x70, v254
	v_bitop3_b32 v2, v196, v7, v2 bitop3:0xde
	s_cmp_lg_u32 0, -1
	v_bfe_u32 v4, v254, 5, 1
	s_cselect_b32 s0, 0, 0
	v_and_b32_e32 v3, 63, v254
	v_lshlrev_b32_e32 v199, 2, v4
	v_sub_u32_e32 v210, v194, v199
	v_cmp_gt_u32_e64 s[4:5], 32, v3
	v_and_b32_e32 v3, 1, v254
	s_mov_b32 s38, 0
	v_cmp_eq_u32_e64 s[6:7], 0, v3
	v_lshlrev_b32_e32 v200, 14, v4
	v_mov_b32_e32 v201, v197
	s_waitcnt vmcnt(11)
	ds_write_b128 v9, v[98:101] offset:32768
	s_waitcnt vmcnt(10)
	ds_write_b128 v9, v[102:105] offset:40960
	v_bfe_u32 v9, v0, 5, 2
	v_or_b32_e32 v8, v8, v9
	v_or_b32_e32 v5, v5, v9
	v_lshlrev_b32_e32 v8, 9, v8
	v_lshlrev_b32_e32 v5, 9, v5
	v_or3_b32 v8, v8, v6, v10
	v_or3_b32 v5, v5, v6, v10
	v_lshlrev_b32_e32 v6, 4, v254
	v_lshlrev_b32_e32 v9, 1, v254
	v_and_b32_e32 v7, 0xc0, v6
	v_and_b32_e32 v9, 32, v9
	v_and_b32_e32 v0, 0x118, v0
	v_or3_b32 v0, v9, v7, v0
	v_add_u32_e32 v211, s0, v0
	v_lshlrev_b32_e32 v0, 4, v4
	v_and_b32_e32 v6, 0x70, v6
	v_xad_u32 v9, v0, v6, 0
	v_or_b32_e32 v10, 32, v0
	v_or_b32_e32 v11, 64, v0
	v_or_b32_e32 v0, 0x60, v0
	v_xad_u32 v10, v10, v6, 0
	v_xad_u32 v11, v11, v6, 0
	v_xad_u32 v6, v0, v6, 0
	v_lshlrev_b32_e32 v0, 3, v4
	v_lshlrev_b32_e32 v7, 8, v194
	v_lshlrev_b32_e32 v202, 1, v0
	v_mbcnt_lo_u32_b32 v0, -1, 0
	v_add_u32_e32 v212, 0xfffffd45, v210
	s_movk_i32 s39, 0x200
	s_movk_i32 s40, 0xfdff
	s_mov_b32 s41, 0x41000000
	s_mov_b32 s12, 0x3e0293ee
	v_mbcnt_hi_u32_b32 v213, -1, v0
	v_lshlrev_b32_e32 v204, 1, v194
	v_add_u32_e32 v214, 0, v8
	v_add_u32_e32 v215, 0, v5
	v_add_u32_e32 v216, v9, v7
	v_add_u32_e32 v217, v10, v7
	v_add_u32_e32 v218, v11, v7
	v_add_u32_e32 v219, v6, v7
	v_mov_b32_e32 v220, 0xff800000
	v_add_u32_e32 v221, 0, v2
	v_mov_b32_e32 v222, 0xf149f2ca
	s_waitcnt lgkmcnt(0)
	s_barrier
	v_readfirstlane_b32 s0, v254
	s_nop 3
	s_lshr_b32 s0, s0, 6
	s_cmp_lt_u32 s0, 4
	s_cbranch_scc1 .Lprio_fa0_done
	s_setprio 1
.Lprio_fa0_done:
	s_branch .LBB0_594

.LBB0_765:
	s_setprio 0
	s_cmpk_lg_i32 s88, 0x100
	s_cbranch_scc1 .Lc3_done
	s_cmpk_gt_i32 s82, 0x7f
	s_cbranch_scc1 .Lc3_done
	s_cmp_lg_u32 s89, 0
	s_cbranch_scc1 .Lc3_done
	v_and_b32_e32 v1, 63, v254
	s_mov_b32 s15, 0
	s_movk_i32 s99, 0x80
	s_sub_i32 s0, s82, s15
	s_lshl_b32 s25, s0, 3
	s_add_i32 s25, s25, s92
	s_cmpk_gt_u32 s25, 0xfff
	s_cbranch_scc1 .Lc3_done
	s_sub_i32 s0, s99, s15
	s_lshl_b32 s8, s0, 3
	s_add_u32 s9, s86, 0x50000000
	s_mul_i32 s0, s92, 0x4100
	s_addc_u32 s10, s87, 0
	s_load_dwordx2 s[4:5], s[90:91], 0xa0
	s_load_dwordx2 s[6:7], s[90:91], 0xb0
	s_add_i32 s2, s0, 0
	s_lshl_b32 s0, s25, 6
	s_lshl_b32 s1, s25, 5
	s_and_b32 s1, s1, 0x780
	s_and_b32 s0, s0, 64
	v_lshlrev_b32_e32 v0, 2, v1
	s_or_b32 s0, s1, s0
	s_waitcnt vmcnt(3)
	v_and_b32_e32 v142, 60, v0
	v_or_b32_e32 v0, s0, v142
	v_readlane_b32 s0, v255, 4
	s_bitcmp0_b32 s0, 7
	s_waitcnt lgkmcnt(0)
	s_cselect_b32 s1, s5, s7
	s_cselect_b32 s0, s4, s6
	s_lshl_b32 s3, s25, 13
	s_and_b32 s3, s3, 0x1f000000
	s_add_u32 s0, s0, s3
	s_addc_u32 s1, s1, 0
	s_and_b32 s3, s25, 0x7c0
	v_lshrrev_b32_e32 v143, 4, v1
	s_waitcnt vmcnt(0)
	v_or_b32_e32 v4, s3, v143
	v_lshlrev_b32_e32 v130, 2, v0
	v_mov_b32_e32 v131, 0
	v_lshl_add_u64 v[2:3], s[0:1], 0, v[130:131]
	v_lshlrev_b32_e32 v130, 13, v4
	v_lshl_add_u64 v[2:3], v[2:3], 0, v[130:131]
	s_mov_b32 s11, 0x8000
	v_add_co_u32_e32 v4, vcc, s11, v2
	s_mov_b32 s12, 0x10000
	s_nop 0
	v_addc_co_u32_e32 v5, vcc, 0, v3, vcc
	global_load_dwordx4 v[66:69], v[2:3], off nt
	global_load_dwordx4 v[70:73], v[4:5], off nt
	v_add_co_u32_e32 v4, vcc, s12, v2
	s_mov_b32 s13, 0x18000
	s_nop 0
	v_addc_co_u32_e32 v5, vcc, 0, v3, vcc
	v_add_co_u32_e32 v6, vcc, s13, v2
	s_mov_b32 s14, 0x20000
	s_nop 0
	v_addc_co_u32_e32 v7, vcc, 0, v3, vcc
	global_load_dwordx4 v[74:77], v[4:5], off nt
	global_load_dwordx4 v[78:81], v[6:7], off nt
	v_add_co_u32_e32 v4, vcc, s14, v2
	s_mov_b32 s16, 0x28000
	s_nop 0
	v_addc_co_u32_e32 v5, vcc, 0, v3, vcc
	v_add_co_u32_e32 v6, vcc, s16, v2
	s_mov_b32 s17, 0x30000
	s_nop 0
	v_addc_co_u32_e32 v7, vcc, 0, v3, vcc
	global_load_dwordx4 v[82:85], v[4:5], off nt
	global_load_dwordx4 v[86:89], v[6:7], off nt
	v_add_co_u32_e32 v4, vcc, s17, v2
	s_mov_b32 s18, 0x38000
	s_nop 0
	v_addc_co_u32_e32 v5, vcc, 0, v3, vcc
	v_add_co_u32_e32 v6, vcc, s18, v2
	s_mov_b32 s19, 0x40000
	s_nop 0
	v_addc_co_u32_e32 v7, vcc, 0, v3, vcc
	global_load_dwordx4 v[90:93], v[4:5], off nt
	global_load_dwordx4 v[94:97], v[6:7], off nt
	v_add_co_u32_e32 v4, vcc, s19, v2
	s_mov_b32 s20, 0x48000
	s_nop 0
	v_addc_co_u32_e32 v5, vcc, 0, v3, vcc
	v_add_co_u32_e32 v6, vcc, s20, v2
	s_mov_b32 s21, 0x50000
	s_nop 0
	v_addc_co_u32_e32 v7, vcc, 0, v3, vcc
	global_load_dwordx4 v[98:101], v[4:5], off nt
	global_load_dwordx4 v[102:105], v[6:7], off nt
	v_add_co_u32_e32 v4, vcc, s21, v2
	s_mov_b32 s22, 0x58000
	s_nop 0
	v_addc_co_u32_e32 v5, vcc, 0, v3, vcc
	v_add_co_u32_e32 v6, vcc, s22, v2
	s_mov_b32 s0, 0x60000
	s_nop 0
	v_addc_co_u32_e32 v7, vcc, 0, v3, vcc
	global_load_dwordx4 v[106:109], v[4:5], off nt
	global_load_dwordx4 v[110:113], v[6:7], off nt
	v_add_co_u32_e32 v4, vcc, s0, v2
	s_mov_b32 s0, 0x68000
	s_nop 0
	v_addc_co_u32_e32 v5, vcc, 0, v3, vcc
	v_add_co_u32_e32 v6, vcc, s0, v2
	s_mov_b32 s0, 0x70000
	s_nop 0
	v_addc_co_u32_e32 v7, vcc, 0, v3, vcc
	global_load_dwordx4 v[114:117], v[4:5], off nt
	global_load_dwordx4 v[118:121], v[6:7], off nt
	v_add_co_u32_e32 v4, vcc, s0, v2
	s_mov_b32 s0, 0x78000
	s_nop 0
	v_addc_co_u32_e32 v5, vcc, 0, v3, vcc
	v_add_co_u32_e32 v2, vcc, s0, v2
	s_lshl_b32 s0, s15, 3
	s_nop 0
	v_addc_co_u32_e32 v3, vcc, 0, v3, vcc
	global_load_dwordx4 v[122:125], v[4:5], off nt
	global_load_dwordx4 v[126:129], v[2:3], off nt
	s_sub_i32 s23, 0, s0
	s_lshl_b32 s0, s82, 3
	v_lshlrev_b32_e32 v3, 4, v1
	s_add_i32 s24, s92, s0
	s_lshl_b32 s0, s99, 7
	s_lshl_b32 s1, s15, 7
	v_and_b32_e32 v132, 48, v3
	s_sub_i32 s26, s0, s1
	s_lshl_b32 s0, s99, 3
	s_lshl_b32 s1, s15, 4
	v_mul_u32_u24_e32 v3, 0x104, v132
	v_and_b32_e32 v4, 60, v1
	s_sub_i32 s27, s0, s1
	s_add_i32 s0, s24, s0
	v_add3_u32 v144, s2, v3, v4
	v_lshlrev_b32_e32 v3, 5, v1
	s_sub_i32 s0, s0, s1
	v_lshl_add_u32 v0, v142, 2, s2
	v_mul_u32_u24_e32 v2, 0x104, v143
	v_and_b32_e32 v134, 0x780, v3
	s_lshl_b32 s28, s0, 6
	s_lshl_b32 s0, s99, 9
	s_lshl_b32 s1, s15, 9
	v_mov_b32_e32 v133, v131
	v_mov_b32_e32 v135, v131
	v_or_b32_e32 v136, 0x800, v134
	v_mov_b32_e32 v137, v131
	v_or_b32_e32 v138, 0x1000, v134
	v_mov_b32_e32 v139, v131
	v_or_b32_e32 v140, 0x1800, v134
	v_mov_b32_e32 v141, v131
	s_lshl_b32 s25, s25, 4
	s_sub_i32 s15, s0, s1
	v_add_u32_e32 v145, v0, v2
	s_branch .Lc3_1000

.LBB0_815:
	s_cmp_gt_i32 s72, 4
	s_cselect_b64 s[0:1], -1, 0
	s_cmp_lt_i32 s73, 5
	s_cselect_b64 s[2:3], -1, 0
	s_or_b64 s[0:1], s[0:1], s[2:3]
	s_and_b64 vcc, exec, s[0:1]
	s_cbranch_vccnz .LBB0_1057
	v_mov_b32_e32 v0, v254
	s_waitcnt lgkmcnt(0)
	s_cmp_eq_u32 s89, 2
	v_and_b32_e32 v1, 63, v0
	s_mov_b64 s[4:5], -1
	s_cbranch_scc1 .LBB0_1003
	s_min_i32 s15, s88, 0xab
	s_cmp_ge_i32 s82, s15
	s_cselect_b64 s[10:11], -1, 0
	s_and_b64 vcc, exec, s[10:11]
	s_cbranch_vccnz .LBB0_992
	s_ashr_i32 s0, s82, 3
	s_lshr_b32 s1, s0, 28
	s_add_i32 s1, s0, s1
	s_ashr_i32 s2, s1, 4
	s_and_b32 s1, s1, -16
	s_sub_i32 s0, s0, s1
	s_ashr_i32 s1, s0, 31
	s_lshr_b32 s1, s1, 28
	s_add_i32 s1, s0, s1
	s_ashr_i32 s3, s1, 4
	s_and_b32 s1, s1, -16
	s_sub_i32 s0, s0, s1
	s_sub_i32 s33, 31, s0
	s_cmp_lt_i32 s0, 0
	s_cselect_b32 s12, s33, s0
	s_lshl_b32 s0, s2, 3
	s_and_b32 s1, s82, 7
	s_or_b32 s0, s0, s1
	s_add_i32 s36, s0, s3
	s_ashr_i32 s0, s36, 2
	s_ashr_i32 s1, s0, 31
	s_ashr_i32 s13, s12, 31
	s_and_b32 s6, s36, 3
	s_lshl_b64 s[2:3], s[0:1], 11
	s_lshl_b64 s[4:5], s[12:13], 6
	s_add_u32 s2, s2, s4
	s_addc_u32 s3, s3, s5
	s_mul_i32 s1, s3, 0x8a00
	s_mul_hi_u32 s4, s2, 0x8a00
	s_add_i32 s4, s4, s1
	s_mul_i32 s1, s2, 0x8a00
	s_add_u32 s1, s96, s1
	s_addc_u32 s4, s97, s4
	s_lshl_b32 s5, s6, 10
	s_add_u32 s1, s1, s5
	s_addc_u32 s4, s4, 0
	s_add_u32 s39, s1, 0x4000
	s_addc_u32 s40, s4, 0
	s_mul_hi_i32 s1, s0, 0x4500000
	s_mul_i32 s0, s0, 0x4500000
	s_add_u32 s0, s96, s0
	s_addc_u32 s1, s97, s1
	s_lshl_b32 s4, s6, 8
	s_add_u32 s0, s0, s4
	s_addc_u32 s1, s1, 0
	s_add_u32 s28, s0, 0x5800
	s_addc_u32 s29, s1, 0
	s_add_u32 s30, s0, 0x5c00
	s_addc_u32 s31, s1, 0
	s_add_u32 s37, s86, 0x31800000
	s_addc_u32 s38, s87, 0
	s_lshl_b64 s[0:1], s[2:3], 12
	s_add_u32 s0, s37, s0
	s_addc_u32 s1, s38, s1
	s_add_u32 s26, s0, s5
	s_addc_u32 s27, s1, 0
	s_add_u32 s41, s86, 0x900000
	s_addc_u32 s42, s87, 0
	s_lshl_b64 s[0:1], s[2:3], 4
	s_add_u32 s0, s41, s0
	s_addc_u32 s1, s42, s1
	s_lshl_b32 s2, s6, 2
	s_add_u32 s8, s0, s2
	v_readfirstlane_b32 s2, v254
	s_addc_u32 s9, s1, 0
	s_and_b32 s0, s2, 0xffffff80
	v_and_b32_e32 v194, 31, v254
	s_ashr_i32 s1, s0, 31
	s_lshr_b32 s2, s2, 1
	s_lshl_b32 s53, s12, 6
	v_and_or_b32 v0, s2, 32, v194
	s_lshl_b64 s[0:1], s[0:1], 1
	v_mul_u32_u24_e32 v0, 0x4500, v0
	s_add_u32 s0, s39, s0
	s_addc_u32 s1, s40, s1
	v_lshlrev_b32_e32 v196, 1, v0
	v_mov_b32_e32 v197, 0
	s_waitcnt vmcnt(0)
	v_lshl_add_u64 v[2:3], s[0:1], 0, v[196:197]
	s_add_i32 s0, s53, 0xfffff801
	s_andn2_b32 s0, s0, 63
	s_cmp_gt_i32 s12, 31
	v_lshrrev_b32_e32 v0, 1, v254
	s_cselect_b32 s0, s0, 0
	v_lshrrev_b32_e32 v195, 4, v254
	v_lshlrev_b32_e32 v8, 3, v254
	s_mov_b32 s13, 0x8a00
	v_and_b32_e32 v196, 16, v0
	v_and_b32_e32 v0, 0x78, v8
	v_or_b32_e32 v9, s0, v195
	v_or_b32_e32 v213, 32, v195
	v_mov_b64_e32 v[4:5], s[28:29]
	v_lshl_add_u64 v[2:3], v[2:3], 0, v[196:197]
	v_lshlrev_b32_e32 v196, 1, v0
	v_or_b32_e32 v10, s0, v213
	v_mad_u64_u32 v[6:7], s[0:1], v9, s13, v[4:5]
	v_lshl_add_u64 v[6:7], v[6:7], 0, v[196:197]
	v_mad_u64_u32 v[4:5], s[0:1], v10, s13, v[4:5]
	v_lshl_add_u64 v[4:5], v[4:5], 0, v[196:197]
	global_load_dwordx4 v[98:101], v[6:7], off
	global_load_dwordx4 v[102:105], v[4:5], off
	global_load_dwordx4 v[158:161], v[2:3], off
	global_load_dwordx4 v[154:157], v[2:3], off offset:32
	global_load_dwordx4 v[150:153], v[2:3], off offset:64
	global_load_dwordx4 v[146:149], v[2:3], off offset:96
	global_load_dwordx4 v[142:145], v[2:3], off offset:128
	global_load_dwordx4 v[138:141], v[2:3], off offset:160
	global_load_dwordx4 v[134:137], v[2:3], off offset:192
	global_load_dwordx4 v[130:133], v[2:3], off offset:224
	v_mov_b64_e32 v[4:5], s[30:31]
	v_mad_u64_u32 v[2:3], s[0:1], v9, s13, v[4:5]
	v_mad_u64_u32 v[4:5], s[0:1], v10, s13, v[4:5]
	v_lshl_add_u64 v[2:3], v[2:3], 0, v[196:197]
	v_lshl_add_u64 v[4:5], v[4:5], 0, v[196:197]
	global_load_dwordx4 v[106:109], v[2:3], off
	global_load_dwordx4 v[110:113], v[4:5], off
	s_movk_i32 s0, 0x70
	v_lshrrev_b32_e32 v5, 3, v254
	v_lshlrev_b32_e32 v7, 8, v195
	v_and_b32_e32 v5, 8, v5
	v_bitop3_b32 v10, v196, v254, s0 bitop3:0x78
	v_and_or_b32 v9, v195, 16, v5
	v_add3_u32 v10, 0, v7, v10
	v_and_or_b32 v5, v213, 48, v5
	v_lshrrev_b32_e32 v6, 5, v254
	s_waitcnt vmcnt(0)
	v_lshrrev_b32_e32 v9, 1, v9
	v_bfe_u32 v11, v254, 4, 2
	v_lshrrev_b32_e32 v5, 1, v5
	v_and_or_b32 v6, v6, 4, v11
	v_and_b32_e32 v2, 0x70, v254
	v_lshlrev_b32_e32 v6, 6, v6
	v_and_b32_e32 v11, 48, v196
	v_bfe_u32 v4, v254, 5, 1
	s_cmp_lg_u32 0, -1
	v_and_b32_e32 v3, 63, v254
	s_cselect_b32 s0, 0, 0
	v_lshlrev_b32_e32 v210, 2, v4
	v_cmp_gt_u32_e64 s[4:5], 32, v3
	v_and_b32_e32 v3, 1, v254
	s_mov_b32 s43, 0
	v_sub_u32_e32 v211, v194, v210
	v_cmp_eq_u32_e64 s[6:7], 0, v3
	v_lshlrev_b32_e32 v252, 14, v4
	v_mov_b32_e32 v253, v197
	s_waitcnt vmcnt(11)
	ds_write_b128 v10, v[98:101] offset:32768
	s_waitcnt vmcnt(10)
	ds_write_b128 v10, v[102:105] offset:40960
	v_bfe_u32 v10, v8, 5, 2
	v_or_b32_e32 v9, v9, v10
	v_or_b32_e32 v5, v5, v10
	v_lshlrev_b32_e32 v9, 9, v9
	v_lshlrev_b32_e32 v5, 9, v5
	v_or3_b32 v9, v9, v6, v11
	v_or3_b32 v5, v5, v6, v11
	v_bitop3_b32 v6, v196, v7, v2 bitop3:0xde
	v_lshlrev_b32_e32 v2, 4, v254
	v_lshlrev_b32_e32 v10, 1, v254
	v_and_b32_e32 v7, 0xc0, v2
	v_and_b32_e32 v10, 32, v10
	v_and_b32_e32 v8, 0x118, v8
	v_or3_b32 v7, v10, v7, v8
	v_lshlrev_b32_e32 v8, 4, v4
	v_and_b32_e32 v2, 0x70, v2
	v_xad_u32 v10, v8, v2, 0
	v_or_b32_e32 v11, 32, v8
	v_or_b32_e32 v12, 64, v8
	v_or_b32_e32 v8, 0x60, v8
	v_xad_u32 v11, v11, v2, 0
	v_xad_u32 v12, v12, v2, 0
	v_xad_u32 v8, v8, v2, 0
	v_lshlrev_b32_e32 v2, 3, v4
	v_add_u32_e32 v212, s0, v7
	v_lshlrev_b32_e32 v7, 8, v194
	v_lshlrev_b32_e32 v202, 1, v2
	v_mbcnt_lo_u32_b32 v2, -1, 0
	s_mov_b32 s44, 0x41000000
	s_mov_b32 s14, 0x3e0293ee
	v_mbcnt_hi_u32_b32 v214, -1, v2
	v_lshlrev_b32_e32 v204, 1, v194
	v_add_u32_e32 v215, 0, v9
	v_add_u32_e32 v216, 0, v5
	v_add_u32_e32 v217, v10, v7
	v_add_u32_e32 v218, v11, v7
	v_add_u32_e32 v219, v12, v7
	v_add_u32_e32 v220, v8, v7
	v_mov_b32_e32 v221, 0xff800000
	v_add_u32_e32 v222, 0, v6
	v_mov_b32_e32 v223, 0xf149f2ca
	s_mov_b32 s45, s82
	s_waitcnt lgkmcnt(0)
	s_barrier
	v_readfirstlane_b32 s0, v254
	s_nop 3
	s_lshr_b32 s0, s0, 6
	s_cmp_lt_u32 s0, 4
	s_cbranch_scc1 .Lprio_fa1_done
	s_setprio 1

.LBB0_992:
	s_setprio 0
	s_cmp_lt_i32 s89, 1
	s_cbranch_scc1 .LBB0_994
	s_cmp_lg_u32 s89, 1
	s_cselect_b64 s[4:5], -1, 0
	s_cbranch_execz .LBB0_995
	s_branch .LBB0_1003
